# MLA MFMA streams at priority 1 with a brief drop every 4 MFMAs
# speedup vs baseline: 1.0056x; 1.0002x over previous
.Lb2:
	s_setprio 1
	s_add_i32 s14, s10, -2
	s_and_b32 s14, s14, 3
	s_mulk_i32 s14, 0x6000
	v_add_u32_e32 v146, s14, v147
	v_add_u32_e32 v161, s14, v148
	v_add_u32_e32 v144, s14, v149
	v_add_u32_e32 v168, s14, v150
	s_waitcnt lgkmcnt(14)
	v_mfma_f32_32x32x16_bf16 v[48:63], v[224:227], v[76:79], v[48:63]
	ds_read_b64_tr_b16 v[224:225], v166
	ds_read_b64_tr_b16 v[226:227], v167 offset:768
	s_waitcnt lgkmcnt(14)
	v_mfma_f32_32x32x16_bf16 v[0:15], v[228:231], v[76:79], v[0:15]
	ds_read_b64_tr_b16 v[228:229], v166 offset:128
	ds_read_b64_tr_b16 v[230:231], v167 offset:896
	s_waitcnt lgkmcnt(14)
	v_mfma_f32_32x32x16_bf16 v[48:63], v[232:235], v[72:75], v[48:63]
	ds_read_b64_tr_b16 v[232:233], v166 offset:6144
	ds_read_b64_tr_b16 v[234:235], v167 offset:6912
	s_waitcnt lgkmcnt(14)
	v_mfma_f32_32x32x16_bf16 v[0:15], v[236:239], v[72:75], v[0:15]
	s_setprio 0
	s_setprio 1
	ds_read_b64_tr_b16 v[236:237], v166 offset:6272
	ds_read_b64_tr_b16 v[238:239], v167 offset:7040
	s_waitcnt lgkmcnt(14)
	v_mfma_f32_32x32x16_bf16 v[48:63], v[240:243], v[64:67], v[48:63]
	ds_read_b64_tr_b16 v[240:241], v166 offset:12288
	ds_read_b64_tr_b16 v[242:243], v167 offset:13056
	s_waitcnt lgkmcnt(14)
	v_mfma_f32_32x32x16_bf16 v[0:15], v[244:247], v[64:67], v[0:15]
	ds_read_b64_tr_b16 v[244:245], v166 offset:12416
	ds_read_b64_tr_b16 v[246:247], v167 offset:13184
	s_waitcnt lgkmcnt(14)
	v_mfma_f32_32x32x16_bf16 v[48:63], v[252:255], v[68:71], v[48:63]
	ds_read_b64_tr_b16 v[252:253], v166 offset:18432
	ds_read_b64_tr_b16 v[254:255], v167 offset:19200
	s_waitcnt lgkmcnt(14)
	v_mfma_f32_32x32x16_bf16 v[0:15], v[204:207], v[68:71], v[0:15]
	s_setprio 0
	s_setprio 1
	ds_read_b64_tr_b16 v[204:205], v166 offset:18560
	ds_read_b64_tr_b16 v[206:207], v167 offset:19328
	s_waitcnt lgkmcnt(14)
	v_mfma_f32_32x32x16_bf16 v[32:47], v[224:227], v[76:79], v[32:47]
	ds_read_b128 v[224:227], v146
	s_waitcnt lgkmcnt(13)
	v_mfma_f32_32x32x16_bf16 v[16:31], v[228:231], v[76:79], v[16:31]
	ds_read_b128 v[228:231], v146 offset:12288
	s_waitcnt lgkmcnt(12)
	v_mfma_f32_32x32x16_bf16 v[32:47], v[232:235], v[72:75], v[32:47]
	ds_read_b128 v[232:235], v161
	s_waitcnt lgkmcnt(11)
	v_mfma_f32_32x32x16_bf16 v[16:31], v[236:239], v[72:75], v[16:31]
	s_setprio 0
	s_setprio 1
	ds_read_b128 v[236:239], v161 offset:12288
	s_waitcnt lgkmcnt(10)
	v_mfma_f32_32x32x16_bf16 v[32:47], v[240:243], v[64:67], v[32:47]
	ds_read_b128 v[240:243], v144
	s_waitcnt lgkmcnt(9)
	v_mfma_f32_32x32x16_bf16 v[16:31], v[244:247], v[64:67], v[16:31]
	ds_read_b128 v[244:247], v144 offset:12288
	s_waitcnt lgkmcnt(8)
	v_mfma_f32_32x32x16_bf16 v[32:47], v[252:255], v[68:71], v[32:47]
	ds_read_b128 v[252:255], v168
	s_waitcnt lgkmcnt(7)
	v_mfma_f32_32x32x16_bf16 v[16:31], v[204:207], v[68:71], v[16:31]
	s_setprio 0
	s_setprio 1
	ds_read_b128 v[204:207], v168 offset:12288
	s_waitcnt lgkmcnt(7)
	v_mfma_f32_32x32x16_bf16 v[80:95], v[224:227], v[112:115], 0
	ds_read_b128 v[224:227], v146 offset:128
	s_waitcnt lgkmcnt(7)
	v_mfma_f32_32x32x16_bf16 v[64:79], v[228:231], v[112:115], 0
	ds_read_b128 v[228:231], v146 offset:12416
	s_waitcnt lgkmcnt(7)
	v_mfma_f32_32x32x16_bf16 v[80:95], v[232:235], v[116:119], v[80:95]
	ds_read_b128 v[232:235], v161 offset:128
	s_waitcnt lgkmcnt(7)
	v_mfma_f32_32x32x16_bf16 v[64:79], v[236:239], v[116:119], v[64:79]
	s_setprio 0
	s_setprio 1
	ds_read_b128 v[236:239], v161 offset:12416
	s_waitcnt lgkmcnt(7)
	v_mfma_f32_32x32x16_bf16 v[80:95], v[240:243], v[120:123], v[80:95]
	ds_read_b128 v[240:243], v144 offset:128
	s_waitcnt lgkmcnt(7)
	v_mfma_f32_32x32x16_bf16 v[64:79], v[244:247], v[120:123], v[64:79]
	ds_read_b128 v[244:247], v144 offset:12416
	s_waitcnt lgkmcnt(7)
	v_mfma_f32_32x32x16_bf16 v[80:95], v[252:255], v[124:127], v[80:95]
	ds_read_b128 v[252:255], v168 offset:128
	s_waitcnt lgkmcnt(7)
	v_mfma_f32_32x32x16_bf16 v[64:79], v[204:207], v[124:127], v[64:79]
	s_setprio 0
	s_setprio 1
	ds_read_b128 v[204:207], v168 offset:12416
	s_waitcnt lgkmcnt(7)
	v_mfma_f32_32x32x16_bf16 v[80:95], v[224:227], v[96:99], v[80:95]
	ds_read_b128 v[224:227], v146 offset:256
	s_waitcnt lgkmcnt(7)
	v_mfma_f32_32x32x16_bf16 v[64:79], v[228:231], v[96:99], v[64:79]
	ds_read_b128 v[228:231], v146 offset:12544
	s_waitcnt lgkmcnt(7)
	v_mfma_f32_32x32x16_bf16 v[80:95], v[232:235], v[100:103], v[80:95]
	ds_read_b128 v[232:235], v161 offset:256
	s_waitcnt lgkmcnt(7)
	v_mfma_f32_32x32x16_bf16 v[64:79], v[236:239], v[100:103], v[64:79]
	s_setprio 0
	s_setprio 1
	ds_read_b128 v[236:239], v161 offset:12544
	s_waitcnt lgkmcnt(7)
	v_mfma_f32_32x32x16_bf16 v[80:95], v[240:243], v[104:107], v[80:95]
	ds_read_b128 v[240:243], v144 offset:256
	s_waitcnt lgkmcnt(7)
	v_mfma_f32_32x32x16_bf16 v[64:79], v[244:247], v[104:107], v[64:79]
	ds_read_b128 v[244:247], v144 offset:12544
	s_waitcnt lgkmcnt(7)
	v_mfma_f32_32x32x16_bf16 v[80:95], v[252:255], v[108:111], v[80:95]
	ds_read_b128 v[252:255], v168 offset:256
	s_waitcnt lgkmcnt(7)
	v_mfma_f32_32x32x16_bf16 v[64:79], v[204:207], v[108:111], v[64:79]
	s_setprio 0
	s_setprio 1
	ds_read_b128 v[204:207], v168 offset:12544
	s_waitcnt lgkmcnt(7)
	v_mfma_f32_32x32x16_bf16 v[80:95], v[224:227], v[128:131], v[80:95]
	s_waitcnt lgkmcnt(6)
	v_mfma_f32_32x32x16_bf16 v[64:79], v[228:231], v[128:131], v[64:79]
	s_waitcnt lgkmcnt(5)
	v_mfma_f32_32x32x16_bf16 v[80:95], v[232:235], v[132:135], v[80:95]
	s_waitcnt lgkmcnt(4)
	v_mfma_f32_32x32x16_bf16 v[64:79], v[236:239], v[132:135], v[64:79]
	s_setprio 0
	s_setprio 1
	s_waitcnt lgkmcnt(3)
	v_mfma_f32_32x32x16_bf16 v[80:95], v[240:243], v[136:139], v[80:95]
	s_waitcnt lgkmcnt(2)
	v_mfma_f32_32x32x16_bf16 v[64:79], v[244:247], v[136:139], v[64:79]
	s_waitcnt lgkmcnt(1)
	v_mfma_f32_32x32x16_bf16 v[80:95], v[252:255], v[140:143], v[80:95]
	s_waitcnt lgkmcnt(0)
	v_mfma_f32_32x32x16_bf16 v[64:79], v[204:207], v[140:143], v[64:79]
	s_setprio 0
	s_waitcnt vmcnt(0)
	s_cmp_lt_u32 s88, 0x1000
	s_cbranch_scc1 .Lb3
	s_barrier

.Lb4:
	s_cmp_ge_u32 s13, s9
	s_setprio 1
	v_add_u32_e32 v144, s98, v147
	v_add_u32_e32 v146, s98, v148
	v_add_u32_e32 v161, s98, v149
	v_add_u32_e32 v168, s98, v150
	s_waitcnt lgkmcnt(14)
	v_mfma_f32_32x32x16_bf16 v[48:63], v[224:227], v[72:75], v[48:63]
	ds_read_b64_tr_b16 v[224:225], v213
	ds_read_b64_tr_b16 v[226:227], v214 offset:768
	s_waitcnt lgkmcnt(14)
	v_mfma_f32_32x32x16_bf16 v[0:15], v[228:231], v[72:75], v[0:15]
	ds_read_b64_tr_b16 v[228:229], v213 offset:128
	ds_read_b64_tr_b16 v[230:231], v214 offset:896
	s_waitcnt lgkmcnt(14)
	v_mfma_f32_32x32x16_bf16 v[48:63], v[232:235], v[76:79], v[48:63]
	ds_read_b64_tr_b16 v[232:233], v213 offset:6144
	ds_read_b64_tr_b16 v[234:235], v214 offset:6912
	s_waitcnt lgkmcnt(14)
	v_mfma_f32_32x32x16_bf16 v[0:15], v[236:239], v[76:79], v[0:15]
	s_setprio 0
	s_setprio 1
	ds_read_b64_tr_b16 v[236:237], v213 offset:6272
	ds_read_b64_tr_b16 v[238:239], v214 offset:7040
	s_waitcnt lgkmcnt(14)
	v_mfma_f32_32x32x16_bf16 v[48:63], v[240:243], v[68:71], v[48:63]
	ds_read_b64_tr_b16 v[240:241], v213 offset:12288
	ds_read_b64_tr_b16 v[242:243], v214 offset:13056
	s_waitcnt lgkmcnt(14)
	v_mfma_f32_32x32x16_bf16 v[0:15], v[244:247], v[68:71], v[0:15]
	ds_read_b64_tr_b16 v[244:245], v213 offset:12416
	ds_read_b64_tr_b16 v[246:247], v214 offset:13184
	s_waitcnt lgkmcnt(14)
	v_mfma_f32_32x32x16_bf16 v[48:63], v[252:255], v[64:67], v[48:63]
	ds_read_b64_tr_b16 v[252:253], v213 offset:18432
	ds_read_b64_tr_b16 v[254:255], v214 offset:19200
	s_waitcnt lgkmcnt(14)
	v_mfma_f32_32x32x16_bf16 v[0:15], v[204:207], v[64:67], v[0:15]
	s_setprio 0
	s_setprio 1
	ds_read_b64_tr_b16 v[204:205], v213 offset:18560
	ds_read_b64_tr_b16 v[206:207], v214 offset:19328
	s_waitcnt lgkmcnt(14)
	v_mfma_f32_32x32x16_bf16 v[32:47], v[224:227], v[72:75], v[32:47]
	ds_read_b128 v[224:227], v144
	s_waitcnt lgkmcnt(13)
	v_mfma_f32_32x32x16_bf16 v[16:31], v[228:231], v[72:75], v[16:31]
	ds_read_b128 v[228:231], v144 offset:12288
	s_waitcnt lgkmcnt(12)
	v_mfma_f32_32x32x16_bf16 v[32:47], v[232:235], v[76:79], v[32:47]
	ds_read_b128 v[232:235], v146
	s_waitcnt lgkmcnt(11)
	v_mfma_f32_32x32x16_bf16 v[16:31], v[236:239], v[76:79], v[16:31]
	s_setprio 0
	s_setprio 1
	ds_read_b128 v[236:239], v146 offset:12288
	s_waitcnt lgkmcnt(10)
	v_mfma_f32_32x32x16_bf16 v[32:47], v[240:243], v[68:71], v[32:47]
	ds_read_b128 v[240:243], v161
	s_waitcnt lgkmcnt(9)
	v_mfma_f32_32x32x16_bf16 v[16:31], v[244:247], v[68:71], v[16:31]
	ds_read_b128 v[244:247], v161 offset:12288
	s_waitcnt lgkmcnt(8)
	v_mfma_f32_32x32x16_bf16 v[32:47], v[252:255], v[64:67], v[32:47]
	ds_read_b128 v[252:255], v168
	s_waitcnt lgkmcnt(7)
	v_mfma_f32_32x32x16_bf16 v[16:31], v[204:207], v[64:67], v[16:31]
	s_setprio 0
	s_setprio 1
	ds_read_b128 v[204:207], v168 offset:12288
	s_cbranch_scc1 .LBB0_1250
	s_add_i32 s13, s10, -1
	s_mov_b32 s14, s98
	s_waitcnt lgkmcnt(7)
	v_mfma_f32_32x32x16_bf16 v[80:95], v[224:227], v[112:115], 0
	ds_read_b128 v[224:227], v144 offset:128
	s_waitcnt lgkmcnt(7)
	v_mfma_f32_32x32x16_bf16 v[64:79], v[228:231], v[112:115], 0
	ds_read_b128 v[228:231], v144 offset:12416
	s_waitcnt lgkmcnt(7)
	v_mfma_f32_32x32x16_bf16 v[80:95], v[232:235], v[116:119], v[80:95]
	ds_read_b128 v[232:235], v146 offset:128
	s_waitcnt lgkmcnt(7)
	v_mfma_f32_32x32x16_bf16 v[64:79], v[236:239], v[116:119], v[64:79]
	s_setprio 0
	s_setprio 1
	ds_read_b128 v[236:239], v146 offset:12416
	s_waitcnt lgkmcnt(7)
	v_mfma_f32_32x32x16_bf16 v[80:95], v[240:243], v[120:123], v[80:95]
	ds_read_b128 v[240:243], v161 offset:128
	s_waitcnt lgkmcnt(7)
	v_mfma_f32_32x32x16_bf16 v[64:79], v[244:247], v[120:123], v[64:79]
	ds_read_b128 v[244:247], v161 offset:12416
	s_waitcnt lgkmcnt(7)
	v_mfma_f32_32x32x16_bf16 v[80:95], v[252:255], v[124:127], v[80:95]
	ds_read_b128 v[252:255], v168 offset:128
	s_waitcnt lgkmcnt(7)
	v_mfma_f32_32x32x16_bf16 v[64:79], v[204:207], v[124:127], v[64:79]
	s_setprio 0
	s_setprio 1
	ds_read_b128 v[204:207], v168 offset:12416
	s_waitcnt lgkmcnt(7)
	v_mfma_f32_32x32x16_bf16 v[80:95], v[224:227], v[96:99], v[80:95]
	ds_read_b128 v[224:227], v144 offset:256
	s_waitcnt lgkmcnt(7)
	v_mfma_f32_32x32x16_bf16 v[64:79], v[228:231], v[96:99], v[64:79]
	ds_read_b128 v[228:231], v144 offset:12544
	s_waitcnt lgkmcnt(7)
	v_mfma_f32_32x32x16_bf16 v[80:95], v[232:235], v[100:103], v[80:95]
	ds_read_b128 v[232:235], v146 offset:256
	s_waitcnt lgkmcnt(7)
	v_mfma_f32_32x32x16_bf16 v[64:79], v[236:239], v[100:103], v[64:79]
	s_setprio 0
	s_setprio 1
	ds_read_b128 v[236:239], v146 offset:12544
	s_waitcnt lgkmcnt(7)
	v_mfma_f32_32x32x16_bf16 v[80:95], v[240:243], v[104:107], v[80:95]
	ds_read_b128 v[240:243], v161 offset:256
	s_waitcnt lgkmcnt(7)
	v_mfma_f32_32x32x16_bf16 v[64:79], v[244:247], v[104:107], v[64:79]
	ds_read_b128 v[244:247], v161 offset:12544
	s_waitcnt lgkmcnt(7)
	v_mfma_f32_32x32x16_bf16 v[80:95], v[252:255], v[108:111], v[80:95]
	ds_read_b128 v[252:255], v168 offset:256
	s_waitcnt lgkmcnt(7)
	v_mfma_f32_32x32x16_bf16 v[64:79], v[204:207], v[108:111], v[64:79]
	s_setprio 0
	s_setprio 1
	ds_read_b128 v[204:207], v168 offset:12544
	s_waitcnt lgkmcnt(7)
	v_mfma_f32_32x32x16_bf16 v[80:95], v[224:227], v[128:131], v[80:95]
	s_waitcnt lgkmcnt(6)
	v_mfma_f32_32x32x16_bf16 v[64:79], v[228:231], v[128:131], v[64:79]
	s_waitcnt lgkmcnt(5)
	v_mfma_f32_32x32x16_bf16 v[80:95], v[232:235], v[132:135], v[80:95]
	s_waitcnt lgkmcnt(4)
	v_mfma_f32_32x32x16_bf16 v[64:79], v[236:239], v[132:135], v[64:79]
	s_setprio 0
	s_setprio 1
	s_waitcnt lgkmcnt(3)
	v_mfma_f32_32x32x16_bf16 v[80:95], v[240:243], v[136:139], v[80:95]
	s_waitcnt lgkmcnt(2)
	v_mfma_f32_32x32x16_bf16 v[64:79], v[244:247], v[136:139], v[64:79]
	s_waitcnt lgkmcnt(1)
	v_mfma_f32_32x32x16_bf16 v[80:95], v[252:255], v[140:143], v[80:95]
	s_waitcnt lgkmcnt(0)
	v_mfma_f32_32x32x16_bf16 v[64:79], v[204:207], v[140:143], v[64:79]
	s_setprio 0
	s_waitcnt vmcnt(0)
	s_cmp_lt_u32 s88, 0x1000
	s_cbranch_scc1 .Lb1
	s_barrier
